# attention epilogue: 16 row-per-lane dword stores widened to 4 dwordx4 via v_permlane32_swap pairs (same bytes, same addresses)
# speedup vs baseline: 1.0095x; 1.0095x over previous
.LBB0_324:
	ds_bpermute_b32 v2, v1, v214
	ds_bpermute_b32 v4, v1, v215
	v_mov_b32_e32 v5, s49
	ds_read_b32 v5, v5
	v_ashrrev_i32_e32 v197, 31, v196
	s_waitcnt lgkmcnt(2)
	v_add_f32_e32 v2, v214, v2
	v_div_scale_f32 v6, s[6:7], v2, v2, 1.0
	v_rcp_f32_e32 v7, v6
	v_div_scale_f32 v8, vcc, 1.0, v2, 1.0
	s_waitcnt lgkmcnt(1)
	v_add_f32_e32 v4, v215, v4
	v_fma_f32 v9, -v6, v7, 1.0
	v_fmac_f32_e32 v7, v9, v7
	v_mul_f32_e32 v9, v8, v7
	v_fma_f32 v10, -v6, v9, v8
	v_fmac_f32_e32 v9, v10, v7
	v_fma_f32 v6, -v6, v9, v8
	s_waitcnt lgkmcnt(0)
	v_div_scale_f32 v8, s[6:7], v4, v4, v5
	v_rcp_f32_e32 v10, v8
	v_div_fmas_f32 v6, v6, v7, v9
	v_div_fixup_f32 v2, v6, v2, 1.0
	s_load_dwordx2 s[6:7], s[34:35], 0x58
	v_fma_f32 v6, -v8, v10, 1.0
	v_fmac_f32_e32 v10, v6, v10
	v_div_scale_f32 v6, vcc, v5, v4, v5
	v_mul_f32_e32 v7, v6, v10
	v_fma_f32 v9, -v8, v7, v6
	v_fmac_f32_e32 v7, v9, v10
	v_fma_f32 v6, -v8, v7, v6
	v_div_fmas_f32 v6, v6, v10, v7
	v_div_fixup_f32 v10, v6, v4, v5
	v_mul_f32_e32 v4, v130, v10
	v_fma_f32 v12, v114, v2, -v4
	v_mul_f32_e32 v4, v131, v10
	v_fma_f32 v13, v115, v2, -v4
	v_mul_f32_e32 v4, v132, v10
	v_fma_f32 v14, v116, v2, -v4
	v_mul_f32_e32 v4, v133, v10
	v_fma_f32 v15, v117, v2, -v4
	v_mul_f32_e32 v4, v134, v10
	v_fma_f32 v16, v118, v2, -v4
	v_mul_f32_e32 v4, v135, v10
	v_fma_f32 v17, v119, v2, -v4
	v_mul_f32_e32 v4, v136, v10
	v_fma_f32 v114, v120, v2, -v4
	v_mul_f32_e32 v4, v137, v10
	v_fma_f32 v115, v121, v2, -v4
	v_mul_f32_e32 v4, v138, v10
	v_fma_f32 v116, v122, v2, -v4
	v_mul_f32_e32 v4, v139, v10
	v_fma_f32 v117, v123, v2, -v4
	v_mul_f32_e32 v4, v140, v10
	v_fma_f32 v118, v124, v2, -v4
	v_mul_f32_e32 v4, v141, v10
	v_fma_f32 v119, v125, v2, -v4
	v_mul_f32_e32 v4, v142, v10
	v_fma_f32 v120, v126, v2, -v4
	v_mul_f32_e32 v4, v143, v10
	v_fma_f32 v121, v127, v2, -v4
	v_mul_f32_e32 v4, v144, v10
	v_fma_f32 v122, v128, v2, -v4
	v_mul_f32_e32 v4, v145, v10
	v_fma_f32 v123, v129, v2, -v4
	v_mul_f32_e32 v4, v98, v10
	v_fma_f32 v82, v82, v2, -v4
	v_mul_f32_e32 v4, v99, v10
	v_fma_f32 v83, v83, v2, -v4
	v_mul_f32_e32 v4, v100, v10
	v_fma_f32 v84, v84, v2, -v4
	v_mul_f32_e32 v4, v101, v10
	v_fma_f32 v85, v85, v2, -v4
	v_mul_f32_e32 v4, v102, v10
	v_fma_f32 v86, v86, v2, -v4
	v_mul_f32_e32 v4, v103, v10
	v_fma_f32 v87, v87, v2, -v4
	v_mul_f32_e32 v4, v104, v10
	v_fma_f32 v88, v88, v2, -v4
	v_mul_f32_e32 v4, v105, v10
	v_fma_f32 v89, v89, v2, -v4
	v_mul_f32_e32 v4, v106, v10
	v_fma_f32 v90, v90, v2, -v4
	v_mul_f32_e32 v4, v107, v10
	v_fma_f32 v91, v91, v2, -v4
	v_mul_f32_e32 v4, v108, v10
	v_fma_f32 v92, v92, v2, -v4
	v_mul_f32_e32 v4, v109, v10
	v_fma_f32 v93, v93, v2, -v4
	v_mul_f32_e32 v4, v110, v10
	v_fma_f32 v94, v94, v2, -v4
	v_mul_f32_e32 v4, v111, v10
	v_fma_f32 v95, v95, v2, -v4
	v_mul_f32_e32 v4, v112, v10
	v_fma_f32 v96, v96, v2, -v4
	v_mul_f32_e32 v4, v113, v10
	v_fma_f32 v97, v97, v2, -v4
	v_mul_f32_e32 v4, v66, v10
	v_mul_f32_e32 v11, v13, v13
	v_fma_f32 v50, v50, v2, -v4
	v_mul_f32_e32 v4, v67, v10
	v_fmac_f32_e32 v11, v12, v12
	v_fma_f32 v51, v51, v2, -v4
	v_mul_f32_e32 v4, v68, v10
	v_fmac_f32_e32 v11, v14, v14
	v_fma_f32 v52, v52, v2, -v4
	v_mul_f32_e32 v4, v69, v10
	v_fmac_f32_e32 v11, v15, v15
	v_fma_f32 v53, v53, v2, -v4
	v_mul_f32_e32 v4, v70, v10
	v_fmac_f32_e32 v11, v16, v16
	v_fma_f32 v54, v54, v2, -v4
	v_mul_f32_e32 v4, v71, v10
	v_fmac_f32_e32 v11, v17, v17
	v_fma_f32 v55, v55, v2, -v4
	v_mul_f32_e32 v4, v72, v10
	v_fmac_f32_e32 v11, v114, v114
	v_fma_f32 v56, v56, v2, -v4
	v_mul_f32_e32 v4, v73, v10
	v_fmac_f32_e32 v11, v115, v115
	v_fma_f32 v57, v57, v2, -v4
	v_mul_f32_e32 v4, v74, v10
	v_fmac_f32_e32 v11, v116, v116
	v_fma_f32 v58, v58, v2, -v4
	v_mul_f32_e32 v4, v75, v10
	v_fmac_f32_e32 v11, v117, v117
	v_fma_f32 v59, v59, v2, -v4
	v_mul_f32_e32 v4, v76, v10
	v_fmac_f32_e32 v11, v118, v118
	v_fma_f32 v60, v60, v2, -v4
	v_mul_f32_e32 v4, v77, v10
	v_fmac_f32_e32 v11, v119, v119
	v_fma_f32 v61, v61, v2, -v4
	v_mul_f32_e32 v4, v78, v10
	v_fmac_f32_e32 v11, v120, v120
	v_fma_f32 v62, v62, v2, -v4
	v_mul_f32_e32 v4, v79, v10
	v_fmac_f32_e32 v11, v121, v121
	v_fma_f32 v63, v63, v2, -v4
	v_mul_f32_e32 v4, v80, v10
	v_fmac_f32_e32 v11, v122, v122
	v_fma_f32 v64, v64, v2, -v4
	v_mul_f32_e32 v4, v81, v10
	v_fmac_f32_e32 v11, v123, v123
	v_fma_f32 v65, v65, v2, -v4
	v_mul_f32_e32 v4, v34, v10
	v_fmac_f32_e32 v11, v82, v82
	v_fma_f32 v18, v18, v2, -v4
	v_mul_f32_e32 v4, v35, v10
	v_fmac_f32_e32 v11, v83, v83
	v_fma_f32 v19, v19, v2, -v4
	v_mul_f32_e32 v4, v36, v10
	v_fmac_f32_e32 v11, v84, v84
	v_fma_f32 v20, v20, v2, -v4
	v_mul_f32_e32 v4, v37, v10
	v_fmac_f32_e32 v11, v85, v85
	v_fma_f32 v21, v21, v2, -v4
	v_mul_f32_e32 v4, v38, v10
	v_fmac_f32_e32 v11, v86, v86
	v_fma_f32 v22, v22, v2, -v4
	s_waitcnt lgkmcnt(0)
	v_lshl_add_u64 v[4:5], v[196:197], 2, s[6:7]
	v_fmac_f32_e32 v11, v87, v87
	global_load_dwordx4 v[146:149], v[4:5], off
	global_load_dwordx4 v[150:153], v[4:5], off offset:32
	global_load_dwordx4 v[154:157], v[4:5], off offset:64
	global_load_dwordx4 v[158:161], v[4:5], off offset:96
	global_load_dwordx4 v[162:165], v[4:5], off offset:128
	global_load_dwordx4 v[166:169], v[4:5], off offset:160
	global_load_dwordx4 v[170:173], v[4:5], off offset:192
	global_load_dwordx4 v[174:177], v[4:5], off offset:224
	global_load_dwordx4 v[178:181], v[4:5], off offset:256
	global_load_dwordx4 v[182:185], v[4:5], off offset:288
	global_load_dwordx4 v[186:189], v[4:5], off offset:320
	global_load_dwordx4 v[190:193], v[4:5], off offset:352
	global_load_dwordx4 v[222:225], v[4:5], off offset:384
	global_load_dwordx4 v[226:229], v[4:5], off offset:416
	global_load_dwordx4 v[230:233], v[4:5], off offset:448
	global_load_dwordx4 v[234:237], v[4:5], off offset:480
	v_fmac_f32_e32 v11, v88, v88
	v_fmac_f32_e32 v11, v89, v89
	v_fmac_f32_e32 v11, v90, v90
	v_fmac_f32_e32 v11, v91, v91
	v_fmac_f32_e32 v11, v92, v92
	v_fmac_f32_e32 v11, v93, v93
	v_fmac_f32_e32 v11, v94, v94
	v_fmac_f32_e32 v11, v95, v95
	v_fmac_f32_e32 v11, v96, v96
	v_fmac_f32_e32 v11, v97, v97
	v_fmac_f32_e32 v11, v50, v50
	v_fmac_f32_e32 v11, v51, v51
	v_fmac_f32_e32 v11, v52, v52
	v_fmac_f32_e32 v11, v53, v53
	v_fmac_f32_e32 v11, v54, v54
	v_fmac_f32_e32 v11, v55, v55
	v_fmac_f32_e32 v11, v56, v56
	v_fmac_f32_e32 v11, v57, v57
	v_fmac_f32_e32 v11, v58, v58
	v_fmac_f32_e32 v11, v59, v59
	v_fmac_f32_e32 v11, v60, v60
	v_fmac_f32_e32 v11, v61, v61
	v_fmac_f32_e32 v11, v62, v62
	v_fmac_f32_e32 v11, v63, v63
	v_fmac_f32_e32 v11, v64, v64
	v_fmac_f32_e32 v11, v65, v65
	v_fmac_f32_e32 v11, v18, v18
	v_fmac_f32_e32 v11, v19, v19
	v_fmac_f32_e32 v11, v20, v20
	v_fmac_f32_e32 v11, v21, v21
	v_mul_f32_e32 v34, v39, v10
	v_fmac_f32_e32 v11, v22, v22
	v_fma_f32 v23, v23, v2, -v34
	v_mul_f32_e32 v34, v40, v10
	v_fmac_f32_e32 v11, v23, v23
	v_fma_f32 v24, v24, v2, -v34
	v_mul_f32_e32 v34, v41, v10
	v_fmac_f32_e32 v11, v24, v24
	v_fma_f32 v25, v25, v2, -v34
	v_mul_f32_e32 v34, v42, v10
	v_fmac_f32_e32 v11, v25, v25
	v_fma_f32 v26, v26, v2, -v34
	v_mul_f32_e32 v34, v43, v10
	v_fmac_f32_e32 v11, v26, v26
	v_fma_f32 v27, v27, v2, -v34
	v_mul_f32_e32 v34, v44, v10
	v_fmac_f32_e32 v11, v27, v27
	v_fma_f32 v28, v28, v2, -v34
	v_mul_f32_e32 v34, v45, v10
	v_fmac_f32_e32 v11, v28, v28
	v_fma_f32 v29, v29, v2, -v34
	v_mul_f32_e32 v34, v46, v10
	v_fmac_f32_e32 v11, v29, v29
	v_fma_f32 v30, v30, v2, -v34
	v_mul_f32_e32 v34, v47, v10
	v_fmac_f32_e32 v11, v30, v30
	v_fma_f32 v31, v31, v2, -v34
	v_mul_f32_e32 v34, v48, v10
	v_fmac_f32_e32 v11, v31, v31
	v_fma_f32 v32, v32, v2, -v34
	v_mul_f32_e32 v10, v49, v10
	v_fmac_f32_e32 v11, v32, v32
	v_fma_f32 v2, v33, v2, -v10
	v_fmac_f32_e32 v11, v2, v2
	ds_bpermute_b32 v10, v1, v11
	s_mov_b32 s6, 0xf800000
	s_add_i32 s55, s55, 1
	s_waitcnt lgkmcnt(0)
	v_add_f32_e32 v10, v11, v10
	v_mov_b32_e32 v11, 0x3727c5ac
	v_fmamk_f32 v10, v10, 0x3c000000, v11
	v_mul_f32_e32 v11, 0x4f800000, v10
	v_cmp_gt_f32_e32 vcc, s6, v10
	s_nop 1
	v_cndmask_b32_e32 v10, v10, v11, vcc
	v_sqrt_f32_e32 v11, v10
	s_nop 0
	v_add_u32_e32 v33, -1, v11
	v_fma_f32 v34, -v33, v11, v10
	v_cmp_ge_f32_e64 s[8:9], 0, v34
	v_add_u32_e32 v34, 1, v11
	s_nop 0
	v_cndmask_b32_e64 v33, v11, v33, s[8:9]
	v_fma_f32 v11, -v34, v11, v10
	v_cmp_lt_f32_e64 s[8:9], 0, v11
	s_nop 1
	v_cndmask_b32_e64 v11, v33, v34, s[8:9]
	v_mul_f32_e32 v33, 0x37800000, v11
	v_cndmask_b32_e32 v11, v11, v33, vcc
	v_mov_b32_e32 v33, 0x260
	v_cmp_class_f32_e32 vcc, v10, v33
	s_mov_b64 s[8:9], 0
	s_nop 0
	v_cndmask_b32_e32 v10, v11, v10, vcc
	v_div_scale_f32 v11, s[6:7], v10, v10, s54
	v_rcp_f32_e32 v33, v11
	s_nop 0
	v_fma_f32 v34, -v11, v33, 1.0
	v_fmac_f32_e32 v33, v34, v33
	v_div_scale_f32 v34, vcc, s54, v10, s54
	v_mul_f32_e32 v35, v34, v33
	v_fma_f32 v36, -v11, v35, v34
	v_fmac_f32_e32 v35, v36, v33
	v_fma_f32 v11, -v11, v35, v34
	v_div_fmas_f32 v11, v11, v33, v35
	v_div_fixup_f32 v33, v11, v10, s54
	v_mul_f32_e32 v12, v12, v33
	s_waitcnt vmcnt(0)
	v_mul_f32_e32 v6, v146, v12
	v_mul_f32_e32 v12, v13, v33
	v_mul_f32_e32 v7, v147, v12
	v_med3_f32 v6, v6, s48, v202
	v_med3_f32 v7, v7, s48, v202
	v_mov_b32_e32 v238, v3
	v_mul_f32_e32 v12, v14, v33
	v_cvt_pk_fp8_f32 v238, v6, v7
	v_mul_f32_e32 v8, v148, v12
	v_mul_f32_e32 v12, v15, v33
	v_mul_f32_e32 v6, v149, v12
	v_med3_f32 v7, v8, s48, v202
	v_med3_f32 v6, v6, s48, v202
	v_lshlrev_b64 v[10:11], 10, v[194:195]
	v_cvt_pk_fp8_f32 v238, v7, v6 op_sel:[0,0,1]
	v_lshl_add_u64 v[6:7], s[40:41], 0, v[10:11]
	v_lshl_add_u64 v[6:7], v[6:7], 0, s[44:45]
	v_lshl_add_u64 v[6:7], v[6:7], 0, v[196:197]
	v_mul_f32_e32 v12, v16, v33
	v_mov_b32_e32 v239, v3
	v_mul_f32_e32 v14, v121, v33
	v_mul_f32_e32 v15, v122, v33
	v_mul_f32_e32 v16, v123, v33
	v_mul_f32_e32 v2, v2, v33
	v_mul_f32_e32 v8, v150, v12
	v_mul_f32_e32 v12, v17, v33
	v_mul_f32_e32 v9, v151, v12
	v_med3_f32 v8, v8, s48, v202
	v_med3_f32 v9, v9, s48, v202
	v_mul_f32_e32 v12, v114, v33
	v_cvt_pk_fp8_f32 v239, v8, v9
	v_mul_f32_e32 v10, v152, v12
	v_mul_f32_e32 v12, v115, v33
	v_mul_f32_e32 v8, v153, v12
	v_med3_f32 v9, v10, s48, v202
	v_med3_f32 v8, v8, s48, v202
	v_cvt_pk_fp8_f32 v239, v9, v8 op_sel:[0,0,1]
	v_mul_f32_e32 v12, v116, v33
	v_mul_f32_e32 v13, v117, v33
	v_mul_f32_e32 v8, v154, v12
	v_mul_f32_e32 v9, v155, v13
	v_med3_f32 v8, v8, s48, v202
	v_med3_f32 v9, v9, s48, v202
	v_mov_b32_e32 v240, v3
	v_mul_f32_e32 v12, v118, v33
	v_cvt_pk_fp8_f32 v240, v8, v9
	v_mul_f32_e32 v10, v156, v12
	v_mul_f32_e32 v12, v119, v33
	v_mul_f32_e32 v8, v157, v12
	v_med3_f32 v9, v10, s48, v202
	v_med3_f32 v8, v8, s48, v202
	v_cvt_pk_fp8_f32 v240, v9, v8 op_sel:[0,0,1]
	v_mov_b32_e32 v241, v3
	v_mul_f32_e32 v13, v120, v33
	v_mul_f32_e32 v8, v158, v13
	v_mul_f32_e32 v9, v159, v14
	v_med3_f32 v8, v8, s48, v202
	v_med3_f32 v9, v9, s48, v202
	v_cvt_pk_fp8_f32 v241, v8, v9
	v_mul_f32_e32 v10, v160, v15
	v_mul_f32_e32 v8, v161, v16
	v_med3_f32 v9, v10, s48, v202
	v_med3_f32 v8, v8, s48, v202
	v_cvt_pk_fp8_f32 v241, v9, v8 op_sel:[0,0,1]
	v_mul_f32_e32 v13, v82, v33
	v_mul_f32_e32 v14, v83, v33
	v_mul_f32_e32 v15, v84, v33
	v_mov_b32_e32 v242, v3
	v_mul_f32_e32 v16, v85, v33
	v_mul_f32_e32 v8, v162, v13
	v_mul_f32_e32 v9, v163, v14
	v_med3_f32 v8, v8, s48, v202
	v_med3_f32 v9, v9, s48, v202
	v_cvt_pk_fp8_f32 v242, v8, v9
	v_mul_f32_e32 v10, v164, v15
	v_mul_f32_e32 v8, v165, v16
	v_med3_f32 v9, v10, s48, v202
	v_med3_f32 v8, v8, s48, v202
	v_cvt_pk_fp8_f32 v242, v9, v8 op_sel:[0,0,1]
	v_mul_f32_e32 v13, v86, v33
	v_mul_f32_e32 v14, v87, v33
	v_mul_f32_e32 v15, v88, v33
	v_mov_b32_e32 v243, v3
	v_mul_f32_e32 v16, v89, v33
	v_mul_f32_e32 v8, v166, v13
	v_mul_f32_e32 v9, v167, v14
	v_med3_f32 v8, v8, s48, v202
	v_med3_f32 v9, v9, s48, v202
	v_cvt_pk_fp8_f32 v243, v8, v9
	v_mul_f32_e32 v10, v168, v15
	v_mul_f32_e32 v8, v169, v16
	v_med3_f32 v9, v10, s48, v202
	v_med3_f32 v8, v8, s48, v202
	v_cvt_pk_fp8_f32 v243, v9, v8 op_sel:[0,0,1]
	v_mul_f32_e32 v13, v90, v33
	v_mul_f32_e32 v14, v91, v33
	v_mul_f32_e32 v15, v92, v33
	v_mov_b32_e32 v244, v3
	v_mul_f32_e32 v16, v93, v33
	v_mul_f32_e32 v8, v170, v13
	v_mul_f32_e32 v9, v171, v14
	v_med3_f32 v8, v8, s48, v202
	v_med3_f32 v9, v9, s48, v202
	v_cvt_pk_fp8_f32 v244, v8, v9
	v_mul_f32_e32 v10, v172, v15
	v_mul_f32_e32 v8, v173, v16
	v_med3_f32 v9, v10, s48, v202
	v_med3_f32 v8, v8, s48, v202
	v_cvt_pk_fp8_f32 v244, v9, v8 op_sel:[0,0,1]
	v_mul_f32_e32 v13, v94, v33
	v_mul_f32_e32 v14, v95, v33
	v_mul_f32_e32 v15, v96, v33
	v_mov_b32_e32 v245, v3
	v_mul_f32_e32 v16, v97, v33
	v_mul_f32_e32 v8, v174, v13
	v_mul_f32_e32 v9, v175, v14
	v_med3_f32 v8, v8, s48, v202
	v_med3_f32 v9, v9, s48, v202
	v_cvt_pk_fp8_f32 v245, v8, v9
	v_mul_f32_e32 v10, v176, v15
	v_mul_f32_e32 v8, v177, v16
	v_med3_f32 v9, v10, s48, v202
	v_med3_f32 v8, v8, s48, v202
	v_cvt_pk_fp8_f32 v245, v9, v8 op_sel:[0,0,1]
	v_mul_f32_e32 v13, v50, v33
	v_mul_f32_e32 v14, v51, v33
	v_mul_f32_e32 v15, v52, v33
	v_mov_b32_e32 v246, v3
	v_mul_f32_e32 v16, v53, v33
	v_mul_f32_e32 v8, v178, v13
	v_mul_f32_e32 v9, v179, v14
	v_med3_f32 v8, v8, s48, v202
	v_med3_f32 v9, v9, s48, v202
	v_cvt_pk_fp8_f32 v246, v8, v9
	v_mul_f32_e32 v10, v180, v15
	v_mul_f32_e32 v8, v181, v16
	v_med3_f32 v9, v10, s48, v202
	v_med3_f32 v8, v8, s48, v202
	v_cvt_pk_fp8_f32 v246, v9, v8 op_sel:[0,0,1]
	v_mul_f32_e32 v13, v54, v33
	v_mul_f32_e32 v14, v55, v33
	v_mul_f32_e32 v15, v56, v33
	v_mov_b32_e32 v247, v3
	v_mul_f32_e32 v16, v57, v33
	v_mul_f32_e32 v8, v182, v13
	v_mul_f32_e32 v9, v183, v14
	v_med3_f32 v8, v8, s48, v202
	v_med3_f32 v9, v9, s48, v202
	v_cvt_pk_fp8_f32 v247, v8, v9
	v_mul_f32_e32 v10, v184, v15
	v_mul_f32_e32 v8, v185, v16
	v_med3_f32 v9, v10, s48, v202
	v_med3_f32 v8, v8, s48, v202
	v_cvt_pk_fp8_f32 v247, v9, v8 op_sel:[0,0,1]
	v_mul_f32_e32 v13, v58, v33
	v_mul_f32_e32 v14, v59, v33
	v_mul_f32_e32 v15, v60, v33
	v_mov_b32_e32 v248, v3
	v_mul_f32_e32 v16, v61, v33
	v_mul_f32_e32 v8, v186, v13
	v_mul_f32_e32 v9, v187, v14
	v_med3_f32 v8, v8, s48, v202
	v_med3_f32 v9, v9, s48, v202
	v_cvt_pk_fp8_f32 v248, v8, v9
	v_mul_f32_e32 v10, v188, v15
	v_mul_f32_e32 v8, v189, v16
	v_med3_f32 v9, v10, s48, v202
	v_med3_f32 v8, v8, s48, v202
	v_cvt_pk_fp8_f32 v248, v9, v8 op_sel:[0,0,1]
	v_mul_f32_e32 v13, v62, v33
	v_mul_f32_e32 v14, v63, v33
	v_mul_f32_e32 v15, v64, v33
	v_mov_b32_e32 v249, v3
	v_mul_f32_e32 v16, v65, v33
	v_mul_f32_e32 v8, v190, v13
	v_mul_f32_e32 v9, v191, v14
	v_med3_f32 v8, v8, s48, v202
	v_med3_f32 v9, v9, s48, v202
	v_cvt_pk_fp8_f32 v249, v8, v9
	v_mul_f32_e32 v10, v192, v15
	v_mul_f32_e32 v8, v193, v16
	v_med3_f32 v9, v10, s48, v202
	v_med3_f32 v8, v8, s48, v202
	v_cvt_pk_fp8_f32 v249, v9, v8 op_sel:[0,0,1]
	v_mul_f32_e32 v13, v18, v33
	v_mul_f32_e32 v14, v19, v33
	v_mul_f32_e32 v15, v20, v33
	v_mov_b32_e32 v250, v3
	v_mul_f32_e32 v16, v21, v33
	v_mul_f32_e32 v8, v222, v13
	v_mul_f32_e32 v9, v223, v14
	v_med3_f32 v8, v8, s48, v202
	v_med3_f32 v9, v9, s48, v202
	v_cvt_pk_fp8_f32 v250, v8, v9
	v_mul_f32_e32 v10, v224, v15
	v_mul_f32_e32 v8, v225, v16
	v_med3_f32 v9, v10, s48, v202
	v_med3_f32 v8, v8, s48, v202
	v_cvt_pk_fp8_f32 v250, v9, v8 op_sel:[0,0,1]
	v_mul_f32_e32 v13, v22, v33
	v_mul_f32_e32 v14, v23, v33
	v_mul_f32_e32 v15, v24, v33
	v_mov_b32_e32 v251, v3
	v_mul_f32_e32 v16, v25, v33
	v_mul_f32_e32 v8, v226, v13
	v_mul_f32_e32 v9, v227, v14
	v_med3_f32 v8, v8, s48, v202
	v_med3_f32 v9, v9, s48, v202
	v_cvt_pk_fp8_f32 v251, v8, v9
	v_mul_f32_e32 v10, v228, v15
	v_mul_f32_e32 v8, v229, v16
	v_med3_f32 v9, v10, s48, v202
	v_med3_f32 v8, v8, s48, v202
	v_cvt_pk_fp8_f32 v251, v9, v8 op_sel:[0,0,1]
	v_mul_f32_e32 v13, v26, v33
	v_mul_f32_e32 v14, v27, v33
	v_mul_f32_e32 v15, v28, v33
	v_mov_b32_e32 v252, v3
	v_mul_f32_e32 v16, v29, v33
	v_mul_f32_e32 v8, v230, v13
	v_mul_f32_e32 v9, v231, v14
	v_med3_f32 v8, v8, s48, v202
	v_med3_f32 v9, v9, s48, v202
	v_cvt_pk_fp8_f32 v252, v8, v9
	v_mul_f32_e32 v10, v232, v15
	v_mul_f32_e32 v8, v233, v16
	v_med3_f32 v9, v10, s48, v202
	v_med3_f32 v8, v8, s48, v202
	v_cvt_pk_fp8_f32 v252, v9, v8 op_sel:[0,0,1]
	v_mul_f32_e32 v13, v32, v33
	v_mul_f32_e32 v5, v30, v33
	v_mul_f32_e32 v12, v31, v33
	v_mov_b32_e32 v253, v3
	v_mul_f32_e32 v5, v234, v5
	v_mul_f32_e32 v8, v235, v12
	v_med3_f32 v5, v5, s48, v202
	v_med3_f32 v8, v8, s48, v202
	v_cvt_pk_fp8_f32 v253, v5, v8
	v_mul_f32_e32 v9, v236, v13
	v_mul_f32_e32 v2, v237, v2
	v_med3_f32 v5, v9, s48, v202
	v_med3_f32 v2, v2, s48, v202
	v_cvt_pk_fp8_f32 v253, v5, v2 op_sel:[0,0,1]
	v_lshl_add_u64 v[198:199], v[196:197], 1, v[6:7]
	v_lshl_add_u64 v[198:199], v[196:197], 0, v[198:199]
	s_nop 1
	v_permlane32_swap_b32_e32 v238, v239
	v_permlane32_swap_b32_e32 v240, v241
	v_permlane32_swap_b32_e32 v242, v243
	v_permlane32_swap_b32_e32 v244, v245
	v_permlane32_swap_b32_e32 v246, v247
	v_permlane32_swap_b32_e32 v248, v249
	v_permlane32_swap_b32_e32 v250, v251
	v_permlane32_swap_b32_e32 v252, v253
	v_permlane32_swap_b32_e32 v238, v240
	v_permlane32_swap_b32_e32 v239, v241
	v_permlane32_swap_b32_e32 v242, v244
	v_permlane32_swap_b32_e32 v243, v245
	v_permlane32_swap_b32_e32 v246, v248
	v_permlane32_swap_b32_e32 v247, v249
	v_permlane32_swap_b32_e32 v250, v252
	v_permlane32_swap_b32_e32 v251, v253
	s_nop 1
	global_store_dwordx4 v[198:199], v[238:241], off offset:512
	global_store_dwordx4 v[198:199], v[242:245], off offset:544
	global_store_dwordx4 v[198:199], v[246:249], off offset:576
	global_store_dwordx4 v[198:199], v[250:253], off offset:608
	s_barrier
